# phase-3 scan-half workgroups convert 6144 MoE weight items in their slack
# baseline (speedup 1.0000x reference)
.LBB0_765:
	s_cmpk_lg_i32 s88, 0x100
	s_cbranch_scc1 .Lc3_done
	s_cmpk_gt_i32 s82, 0x7f
	s_cbranch_scc1 .Lc3_done
	s_cmp_lg_u32 s89, 0
	s_cbranch_scc1 .Lc3_done
	v_and_b32_e32 v1, 63, v254
	s_mov_b32 s15, 0
	s_movk_i32 s99, 0x80
	s_sub_i32 s0, s82, s15
	s_lshl_b32 s25, s0, 3
	s_add_i32 s25, s25, s92
	s_cmpk_gt_u32 s25, 0x17ff
	s_cbranch_scc1 .Lc3_done
	s_sub_i32 s0, s99, s15
	s_lshl_b32 s8, s0, 3
	s_add_u32 s9, s86, 0x50000000
	s_mul_i32 s0, s92, 0x4100
	s_addc_u32 s10, s87, 0
	s_load_dwordx2 s[4:5], s[90:91], 0xa0
	s_load_dwordx2 s[6:7], s[90:91], 0xb0
	s_add_i32 s2, s0, 0
	s_lshl_b32 s0, s25, 6
	s_lshl_b32 s1, s25, 5
	s_and_b32 s1, s1, 0x780
	s_and_b32 s0, s0, 64
	v_lshlrev_b32_e32 v0, 2, v1
	s_or_b32 s0, s1, s0
	s_waitcnt vmcnt(3)
	v_and_b32_e32 v142, 60, v0
	v_or_b32_e32 v0, s0, v142
	v_readlane_b32 s0, v255, 4
	s_bitcmp0_b32 s0, 7
	s_waitcnt lgkmcnt(0)
	s_cselect_b32 s1, s5, s7
	s_cselect_b32 s0, s4, s6
	s_lshl_b32 s3, s25, 13
	s_and_b32 s3, s3, 0x1f000000
	s_add_u32 s0, s0, s3
	s_addc_u32 s1, s1, 0
	s_and_b32 s3, s25, 0x7c0
	v_lshrrev_b32_e32 v143, 4, v1
	s_waitcnt vmcnt(0)
	v_or_b32_e32 v4, s3, v143
	v_lshlrev_b32_e32 v130, 2, v0
	v_mov_b32_e32 v131, 0
	v_lshl_add_u64 v[2:3], s[0:1], 0, v[130:131]
	v_lshlrev_b32_e32 v130, 13, v4
	v_lshl_add_u64 v[2:3], v[2:3], 0, v[130:131]
	s_mov_b32 s11, 0x8000
	v_add_co_u32_e32 v4, vcc, s11, v2
	s_mov_b32 s12, 0x10000
	s_nop 0
	v_addc_co_u32_e32 v5, vcc, 0, v3, vcc
	global_load_dwordx4 v[66:69], v[2:3], off nt
	global_load_dwordx4 v[70:73], v[4:5], off nt
	v_add_co_u32_e32 v4, vcc, s12, v2
	s_mov_b32 s13, 0x18000
	s_nop 0
	v_addc_co_u32_e32 v5, vcc, 0, v3, vcc
	v_add_co_u32_e32 v6, vcc, s13, v2
	s_mov_b32 s14, 0x20000
	s_nop 0
	v_addc_co_u32_e32 v7, vcc, 0, v3, vcc
	global_load_dwordx4 v[74:77], v[4:5], off nt
	global_load_dwordx4 v[78:81], v[6:7], off nt
	v_add_co_u32_e32 v4, vcc, s14, v2
	s_mov_b32 s16, 0x28000
	s_nop 0
	v_addc_co_u32_e32 v5, vcc, 0, v3, vcc
	v_add_co_u32_e32 v6, vcc, s16, v2
	s_mov_b32 s17, 0x30000
	s_nop 0
	v_addc_co_u32_e32 v7, vcc, 0, v3, vcc
	global_load_dwordx4 v[82:85], v[4:5], off nt
	global_load_dwordx4 v[86:89], v[6:7], off nt
	v_add_co_u32_e32 v4, vcc, s17, v2
	s_mov_b32 s18, 0x38000
	s_nop 0
	v_addc_co_u32_e32 v5, vcc, 0, v3, vcc
	v_add_co_u32_e32 v6, vcc, s18, v2
	s_mov_b32 s19, 0x40000
	s_nop 0
	v_addc_co_u32_e32 v7, vcc, 0, v3, vcc
	global_load_dwordx4 v[90:93], v[4:5], off nt
	global_load_dwordx4 v[94:97], v[6:7], off nt
	v_add_co_u32_e32 v4, vcc, s19, v2
	s_mov_b32 s20, 0x48000
	s_nop 0
	v_addc_co_u32_e32 v5, vcc, 0, v3, vcc
	v_add_co_u32_e32 v6, vcc, s20, v2
	s_mov_b32 s21, 0x50000
	s_nop 0
	v_addc_co_u32_e32 v7, vcc, 0, v3, vcc
	global_load_dwordx4 v[98:101], v[4:5], off nt
	global_load_dwordx4 v[102:105], v[6:7], off nt
	v_add_co_u32_e32 v4, vcc, s21, v2
	s_mov_b32 s22, 0x58000
	s_nop 0
	v_addc_co_u32_e32 v5, vcc, 0, v3, vcc
	v_add_co_u32_e32 v6, vcc, s22, v2
	s_mov_b32 s0, 0x60000
	s_nop 0
	v_addc_co_u32_e32 v7, vcc, 0, v3, vcc
	global_load_dwordx4 v[106:109], v[4:5], off nt
	global_load_dwordx4 v[110:113], v[6:7], off nt
	v_add_co_u32_e32 v4, vcc, s0, v2
	s_mov_b32 s0, 0x68000
	s_nop 0
	v_addc_co_u32_e32 v5, vcc, 0, v3, vcc
	v_add_co_u32_e32 v6, vcc, s0, v2
	s_mov_b32 s0, 0x70000
	s_nop 0
	v_addc_co_u32_e32 v7, vcc, 0, v3, vcc
	global_load_dwordx4 v[114:117], v[4:5], off nt
	global_load_dwordx4 v[118:121], v[6:7], off nt
	v_add_co_u32_e32 v4, vcc, s0, v2
	s_mov_b32 s0, 0x78000
	s_nop 0
	v_addc_co_u32_e32 v5, vcc, 0, v3, vcc
	v_add_co_u32_e32 v2, vcc, s0, v2
	s_lshl_b32 s0, s15, 3
	s_nop 0
	v_addc_co_u32_e32 v3, vcc, 0, v3, vcc
	global_load_dwordx4 v[122:125], v[4:5], off nt
	global_load_dwordx4 v[126:129], v[2:3], off nt
	s_sub_i32 s23, 0, s0
	s_lshl_b32 s0, s82, 3
	v_lshlrev_b32_e32 v3, 4, v1
	s_add_i32 s24, s92, s0
	s_lshl_b32 s0, s99, 7
	s_lshl_b32 s1, s15, 7
	v_and_b32_e32 v132, 48, v3
	s_sub_i32 s26, s0, s1
	s_lshl_b32 s0, s99, 3
	s_lshl_b32 s1, s15, 4
	v_mul_u32_u24_e32 v3, 0x104, v132
	v_and_b32_e32 v4, 60, v1
	s_sub_i32 s27, s0, s1
	s_add_i32 s0, s24, s0
	v_add3_u32 v144, s2, v3, v4
	v_lshlrev_b32_e32 v3, 5, v1
	s_sub_i32 s0, s0, s1
	v_lshl_add_u32 v0, v142, 2, s2
	v_mul_u32_u24_e32 v2, 0x104, v143
	v_and_b32_e32 v134, 0x780, v3
	s_lshl_b32 s28, s0, 6
	s_lshl_b32 s0, s99, 9
	s_lshl_b32 s1, s15, 9
	v_mov_b32_e32 v133, v131
	v_mov_b32_e32 v135, v131
	v_or_b32_e32 v136, 0x800, v134
	v_mov_b32_e32 v137, v131
	v_or_b32_e32 v138, 0x1000, v134
	v_mov_b32_e32 v139, v131
	v_or_b32_e32 v140, 0x1800, v134
	v_mov_b32_e32 v141, v131
	s_lshl_b32 s25, s25, 4
	s_sub_i32 s15, s0, s1
	v_add_u32_e32 v145, v0, v2
	s_branch .Lc3_1000
.Lc3_999:
	v_add_u32_e32 v0, 0x410, v145
	s_waitcnt vmcnt(31)
	ds_write2_b32 v145, v66, v67 offset1:1
	ds_write2_b32 v145, v68, v69 offset0:2 offset1:3
	s_waitcnt vmcnt(30)
	ds_write2_b32 v0, v70, v71 offset1:1
	v_add_u32_e32 v0, 0x418, v145
	ds_write2_b32 v0, v72, v73 offset1:1
	v_add_u32_e32 v0, 0x820, v145
	s_waitcnt vmcnt(29)
	ds_write2_b32 v0, v74, v75 offset1:1
	v_add_u32_e32 v0, 0x828, v145
	ds_write2_b32 v0, v76, v77 offset1:1
	v_add_u32_e32 v0, 0xc30, v145
	s_waitcnt vmcnt(28)
	ds_write2_b32 v0, v78, v79 offset1:1
	v_add_u32_e32 v0, 0xc38, v145
	ds_write2_b32 v0, v80, v81 offset1:1
	v_add_u32_e32 v0, 0x1040, v145
	s_waitcnt vmcnt(27)
	ds_write2_b32 v0, v82, v83 offset1:1
	v_add_u32_e32 v0, 0x1048, v145
	ds_write2_b32 v0, v84, v85 offset1:1
	v_add_u32_e32 v0, 0x1450, v145
	s_waitcnt vmcnt(26)
	ds_write2_b32 v0, v86, v87 offset1:1
	v_add_u32_e32 v0, 0x1458, v145
	ds_write2_b32 v0, v88, v89 offset1:1
	v_add_u32_e32 v0, 0x1860, v145
	s_waitcnt vmcnt(25)
	ds_write2_b32 v0, v90, v91 offset1:1
	v_add_u32_e32 v0, 0x1868, v145
	ds_write2_b32 v0, v92, v93 offset1:1
	v_add_u32_e32 v0, 0x1c70, v145
	s_waitcnt vmcnt(24)
	ds_write2_b32 v0, v94, v95 offset1:1
	v_add_u32_e32 v0, 0x1c78, v145
	ds_write2_b32 v0, v96, v97 offset1:1
	v_add_u32_e32 v0, 0x2080, v145
	s_waitcnt vmcnt(23)
	ds_write2_b32 v0, v98, v99 offset1:1
	v_add_u32_e32 v0, 0x2088, v145
	ds_write2_b32 v0, v100, v101 offset1:1
	v_add_u32_e32 v0, 0x2490, v145
	s_waitcnt vmcnt(22)
	ds_write2_b32 v0, v102, v103 offset1:1
	v_add_u32_e32 v0, 0x2498, v145
	ds_write2_b32 v0, v104, v105 offset1:1
	v_add_u32_e32 v0, 0x28a0, v145
	s_waitcnt vmcnt(21)
	ds_write2_b32 v0, v106, v107 offset1:1
	v_add_u32_e32 v0, 0x28a8, v145
	ds_write2_b32 v0, v108, v109 offset1:1
	v_add_u32_e32 v0, 0x2cb0, v145
	s_waitcnt vmcnt(20)
	ds_write2_b32 v0, v110, v111 offset1:1
	v_add_u32_e32 v0, 0x2cb8, v145
	ds_write2_b32 v0, v112, v113 offset1:1
	v_add_u32_e32 v0, 0x30c0, v145
	s_waitcnt vmcnt(19)
	ds_write2_b32 v0, v114, v115 offset1:1
	v_add_u32_e32 v0, 0x30c8, v145
	ds_write2_b32 v0, v116, v117 offset1:1
	v_add_u32_e32 v0, 0x34d0, v145
	s_waitcnt vmcnt(18)
	ds_write2_b32 v0, v118, v119 offset1:1
	v_add_u32_e32 v0, 0x34d8, v145
	ds_write2_b32 v0, v120, v121 offset1:1
	v_add_u32_e32 v0, 0x38e0, v145
	s_waitcnt vmcnt(17)
	ds_write2_b32 v0, v122, v123 offset1:1
	v_add_u32_e32 v0, 0x38e8, v145
	ds_write2_b32 v0, v124, v125 offset1:1
	v_add_u32_e32 v0, 0x3cf0, v145
	s_waitcnt vmcnt(16)
	ds_write2_b32 v0, v126, v127 offset1:1
	v_add_u32_e32 v0, 0x3cf8, v145
	ds_write2_b32 v0, v128, v129 offset1:1
	s_waitcnt lgkmcnt(0)
	ds_read2_b32 v[70:71], v144 offset1:16
	ds_read2_b32 v[72:73], v144 offset0:65 offset1:81
	ds_read2_b32 v[74:75], v144 offset0:130 offset1:146
	ds_read2_b32 v[76:77], v144 offset0:195 offset1:211
	v_mov_b32_e32 v66, 0
	s_waitcnt lgkmcnt(3)
	v_mul_f32_e32 v0, 0x43800000, v70
	s_waitcnt lgkmcnt(2)
	v_mul_f32_e32 v67, 0x43800000, v72
	v_cvt_pk_fp8_f32 v66, v0, v67
	v_add_u32_e32 v0, 0x400, v144
	ds_read2_b32 v[78:79], v0 offset0:4 offset1:20
	ds_read2_b32 v[80:81], v0 offset0:69 offset1:85
	ds_read2_b32 v[82:83], v0 offset0:134 offset1:150
	s_waitcnt lgkmcnt(4)
	v_mul_f32_e32 v68, 0x43800000, v74
	s_waitcnt lgkmcnt(3)
	v_mul_f32_e32 v67, 0x43800000, v76
	ds_read2_b32 v[84:85], v0 offset0:199 offset1:215
	v_add_u32_e32 v106, 0x800, v144
	v_cvt_pk_fp8_f32 v66, v68, v67 op_sel:[0,0,1]
	s_waitcnt lgkmcnt(3)
	v_mul_f32_e32 v68, 0x43800000, v78
	s_waitcnt lgkmcnt(2)
	v_mul_f32_e32 v69, 0x43800000, v80
	v_mov_b32_e32 v67, 0
	ds_read2_b32 v[86:87], v106 offset0:8 offset1:24
	ds_read2_b32 v[88:89], v106 offset0:73 offset1:89
	v_add_u32_e32 v107, 0xc00, v144
	v_cvt_pk_fp8_f32 v67, v68, v69
	ds_read2_b32 v[90:91], v106 offset0:138 offset1:154
	ds_read2_b32 v[92:93], v106 offset0:203 offset1:219
	ds_read2_b32 v[94:95], v107 offset0:12 offset1:28
	ds_read2_b32 v[96:97], v107 offset0:77 offset1:93
	s_ashr_i32 s0, s29, 11
	s_ashr_i32 s1, s0, 31
	s_lshl_b64 s[0:1], s[0:1], 23
	s_waitcnt lgkmcnt(7)
	v_mul_f32_e32 v70, 0x43800000, v82
	s_waitcnt lgkmcnt(6)
	v_mul_f32_e32 v68, 0x43800000, v84
	s_add_u32 s0, s9, s0
	v_cvt_pk_fp8_f32 v67, v70, v68 op_sel:[0,0,1]
	s_waitcnt lgkmcnt(5)
	v_mul_f32_e32 v69, 0x43800000, v86
	s_waitcnt lgkmcnt(4)
	v_mul_f32_e32 v70, 0x43800000, v88
	v_mov_b32_e32 v68, 0
	ds_read2_b32 v[98:99], v107 offset0:142 offset1:158
	ds_read2_b32 v[100:101], v107 offset0:207 offset1:223
	s_addc_u32 s1, s10, s1
	s_and_b32 s2, s25, 0x3f0
	s_bfe_u32 s3, s29, 0x40007
	v_cvt_pk_fp8_f32 v68, v69, v70
	s_waitcnt lgkmcnt(3)
	v_mul_f32_e32 v70, 0x43800000, v94
	s_waitcnt lgkmcnt(2)
	v_mul_f32_e32 v76, 0x43800000, v96
	v_mov_b32_e32 v69, 0
	s_or_b32 s2, s2, s3
	v_cvt_pk_fp8_f32 v69, v70, v76
	s_lshl_b32 s2, s2, 13
	s_add_u32 s0, s0, s2
	v_mul_f32_e32 v72, 0x43800000, v90
	v_mul_f32_e32 v74, 0x43800000, v92
	s_addc_u32 s1, s1, 0
	s_and_b32 s2, s29, 64
	v_cvt_pk_fp8_f32 v68, v72, v74 op_sel:[0,0,1]
	s_waitcnt lgkmcnt(1)
	v_mul_f32_e32 v70, 0x43800000, v98
	s_waitcnt lgkmcnt(0)
	v_mul_f32_e32 v72, 0x43800000, v100
	s_add_u32 s0, s0, s2
	v_cvt_pk_fp8_f32 v69, v70, v72 op_sel:[0,0,1]
	s_addc_u32 s1, s1, 0
	v_lshl_add_u64 v[102:103], s[0:1], 0, v[132:133]
	v_lshl_add_u64 v[104:105], v[102:103], 0, v[134:135]
	global_store_dwordx4 v[104:105], v[66:69], off nt
	v_mul_f32_e32 v70, 0x43800000, v77
	v_mul_f32_e32 v72, 0x43800000, v93
	v_mul_f32_e32 v67, 0x43800000, v71
	v_mul_f32_e32 v68, 0x43800000, v73
	v_mov_b32_e32 v66, 0
	v_cvt_pk_fp8_f32 v66, v67, v68
	v_mul_f32_e32 v68, 0x43800000, v79
	v_mul_f32_e32 v71, 0x43800000, v81
	v_mov_b32_e32 v67, 0
	v_cvt_pk_fp8_f32 v67, v68, v71
	v_mul_f32_e32 v69, 0x43800000, v75
	v_cvt_pk_fp8_f32 v66, v69, v70 op_sel:[0,0,1]
	v_mul_f32_e32 v68, 0x43800000, v83
	v_mul_f32_e32 v69, 0x43800000, v85
	v_cvt_pk_fp8_f32 v67, v68, v69 op_sel:[0,0,1]
	v_mul_f32_e32 v69, 0x43800000, v87
	v_mul_f32_e32 v70, 0x43800000, v89
	v_mov_b32_e32 v68, 0
	v_cvt_pk_fp8_f32 v68, v69, v70
	v_mul_f32_e32 v70, 0x43800000, v95
	v_mul_f32_e32 v73, 0x43800000, v97
	v_mov_b32_e32 v69, 0
	v_cvt_pk_fp8_f32 v69, v70, v73
	v_mul_f32_e32 v71, 0x43800000, v91
	v_cvt_pk_fp8_f32 v68, v71, v72 op_sel:[0,0,1]
	v_mul_f32_e32 v70, 0x43800000, v99
	v_mul_f32_e32 v71, 0x43800000, v101
	v_cvt_pk_fp8_f32 v69, v70, v71 op_sel:[0,0,1]
	ds_read2_b32 v[70:71], v144 offset0:32 offset1:48
	ds_read2_b32 v[72:73], v144 offset0:97 offset1:113
	ds_read2_b32 v[74:75], v144 offset0:162 offset1:178
	v_lshl_add_u64 v[76:77], v[102:103], 0, v[136:137]
	s_add_i32 s24, s24, s8
	global_store_dwordx4 v[76:77], v[66:69], off nt
	ds_read2_b32 v[76:77], v144 offset0:227 offset1:243
	ds_read2_b32 v[78:79], v0 offset0:36 offset1:52
	ds_read2_b32 v[80:81], v0 offset0:101 offset1:117
	s_waitcnt lgkmcnt(5)
	v_mul_f32_e32 v67, 0x43800000, v70
	s_waitcnt lgkmcnt(4)
	v_mul_f32_e32 v68, 0x43800000, v72
	v_mov_b32_e32 v66, 0
	v_cvt_pk_fp8_f32 v66, v67, v68
	s_waitcnt lgkmcnt(3)
	v_mul_f32_e32 v69, 0x43800000, v74
	s_waitcnt lgkmcnt(2)
	v_mul_f32_e32 v67, 0x43800000, v76
	ds_read2_b32 v[82:83], v0 offset0:166 offset1:182
	ds_read2_b32 v[84:85], v0 offset0:231 offset1:247
	v_cvt_pk_fp8_f32 v66, v69, v67 op_sel:[0,0,1]
	s_waitcnt lgkmcnt(3)
	v_mul_f32_e32 v68, 0x43800000, v78
	s_waitcnt lgkmcnt(2)
	v_mul_f32_e32 v69, 0x43800000, v80
	v_mov_b32_e32 v67, 0
	ds_read2_b32 v[86:87], v106 offset0:40 offset1:56
	v_cvt_pk_fp8_f32 v67, v68, v69
	ds_read2_b32 v[88:89], v106 offset0:105 offset1:121
	ds_read2_b32 v[90:91], v106 offset0:170 offset1:186
	ds_read2_b32 v[92:93], v106 offset0:235 offset1:251
	ds_read2_b32 v[94:95], v107 offset0:44 offset1:60
	ds_read2_b32 v[96:97], v107 offset0:109 offset1:125
	s_waitcnt lgkmcnt(7)
	v_mul_f32_e32 v0, 0x43800000, v82
	s_waitcnt lgkmcnt(6)
	v_mul_f32_e32 v68, 0x43800000, v84
	v_cvt_pk_fp8_f32 v67, v0, v68 op_sel:[0,0,1]
	s_waitcnt lgkmcnt(5)
	v_mul_f32_e32 v0, 0x43800000, v86
	s_waitcnt lgkmcnt(4)
	v_mul_f32_e32 v69, 0x43800000, v88
	v_mov_b32_e32 v68, 0
	ds_read2_b32 v[98:99], v107 offset0:174 offset1:190
	ds_read2_b32 v[100:101], v107 offset0:239 offset1:255
	v_cvt_pk_fp8_f32 v68, v0, v69
	s_waitcnt lgkmcnt(3)
	v_mul_f32_e32 v0, 0x43800000, v94
	s_waitcnt lgkmcnt(2)
	v_mul_f32_e32 v74, 0x43800000, v96
	v_mov_b32_e32 v69, 0
	v_cvt_pk_fp8_f32 v69, v0, v74
	v_mul_f32_e32 v70, 0x43800000, v90
	v_mul_f32_e32 v72, 0x43800000, v92
	v_cvt_pk_fp8_f32 v68, v70, v72 op_sel:[0,0,1]
	s_waitcnt lgkmcnt(1)
	v_mul_f32_e32 v0, 0x43800000, v98
	s_waitcnt lgkmcnt(0)
	v_mul_f32_e32 v70, 0x43800000, v100
	v_cvt_pk_fp8_f32 v69, v0, v70 op_sel:[0,0,1]
	v_mul_f32_e32 v0, 0x43800000, v71
	v_mul_f32_e32 v71, 0x43800000, v73
	v_mov_b32_e32 v70, 0
	v_cvt_pk_fp8_f32 v70, v0, v71
	v_mul_f32_e32 v0, 0x43800000, v79
	v_mul_f32_e32 v74, 0x43800000, v81
	v_mov_b32_e32 v71, 0
	v_cvt_pk_fp8_f32 v71, v0, v74
	v_mul_f32_e32 v72, 0x43800000, v75
	v_mul_f32_e32 v73, 0x43800000, v77
	v_cvt_pk_fp8_f32 v70, v72, v73 op_sel:[0,0,1]
	v_mul_f32_e32 v0, 0x43800000, v83
	v_mul_f32_e32 v72, 0x43800000, v85
	v_cvt_pk_fp8_f32 v71, v0, v72 op_sel:[0,0,1]
	v_mul_f32_e32 v0, 0x43800000, v87
	v_mul_f32_e32 v73, 0x43800000, v89
	v_mov_b32_e32 v72, 0
	v_cvt_pk_fp8_f32 v72, v0, v73
	v_mul_f32_e32 v0, 0x43800000, v95
	v_mul_f32_e32 v76, 0x43800000, v97
	v_mov_b32_e32 v73, 0
	v_cvt_pk_fp8_f32 v73, v0, v76
	v_mul_f32_e32 v74, 0x43800000, v91
	v_mul_f32_e32 v75, 0x43800000, v93
	v_cvt_pk_fp8_f32 v72, v74, v75 op_sel:[0,0,1]
	v_mul_f32_e32 v0, 0x43800000, v99
	v_mul_f32_e32 v74, 0x43800000, v101
	v_cvt_pk_fp8_f32 v73, v0, v74 op_sel:[0,0,1]
	v_lshl_add_u64 v[74:75], v[102:103], 0, v[138:139]
	global_store_dwordx4 v[74:75], v[66:69], off nt
	s_add_i32 s0, s23, s24
	s_add_i32 s25, s25, s26
	v_lshl_add_u64 v[66:67], v[102:103], 0, v[140:141]
	global_store_dwordx4 v[66:67], v[70:73], off nt
	s_waitcnt lgkmcnt(0)
	s_add_i32 s28, s28, s15
	s_waitcnt vmcnt(4)
	v_mov_b64_e32 v[68:69], v[4:5]
	v_mov_b64_e32 v[72:73], v[8:9]
	v_mov_b64_e32 v[76:77], v[12:13]
	v_mov_b64_e32 v[80:81], v[16:17]
	v_mov_b64_e32 v[84:85], v[20:21]
	v_mov_b64_e32 v[88:89], v[24:25]
	v_mov_b64_e32 v[92:93], v[28:29]
	v_mov_b64_e32 v[96:97], v[32:33]
	v_mov_b64_e32 v[100:101], v[36:37]
	v_mov_b64_e32 v[104:105], v[40:41]
	v_mov_b64_e32 v[108:109], v[44:45]
	v_mov_b64_e32 v[112:113], v[48:49]
	v_mov_b64_e32 v[116:117], v[52:53]
	v_mov_b64_e32 v[120:121], v[56:57]
	v_mov_b64_e32 v[124:125], v[60:61]
	v_mov_b64_e32 v[128:129], v[64:65]
	s_cmp_lt_i32 s0, 0x1800
	v_mov_b64_e32 v[66:67], v[2:3]
	v_mov_b64_e32 v[70:71], v[6:7]
	v_mov_b64_e32 v[74:75], v[10:11]
	v_mov_b64_e32 v[78:79], v[14:15]
	v_mov_b64_e32 v[82:83], v[18:19]
	v_mov_b64_e32 v[86:87], v[22:23]
	v_mov_b64_e32 v[90:91], v[26:27]
	v_mov_b64_e32 v[94:95], v[30:31]
	v_mov_b64_e32 v[98:99], v[34:35]
	v_mov_b64_e32 v[102:103], v[38:39]
	v_mov_b64_e32 v[106:107], v[42:43]
	v_mov_b64_e32 v[110:111], v[46:47]
	v_mov_b64_e32 v[114:115], v[50:51]
	v_mov_b64_e32 v[118:119], v[54:55]
	v_mov_b64_e32 v[122:123], v[58:59]
	v_mov_b64_e32 v[126:127], v[62:63]
	s_cbranch_scc0 .Lc3_done
.Lc3_1000:
	s_add_i32 s29, s23, s24
	s_add_i32 s30, s27, s24
	s_cmp_gt_i32 s30, 0x17ff
	s_cbranch_scc1 .Lc3_last
	s_lshr_b32 s1, s28, 1
	s_ashr_i32 s0, s30, 11
	s_and_b32 s2, s1, 0x780
	s_and_b32 s3, s28, 64
	s_bitcmp0_b32 s29, 1
	s_cselect_b32 s31, s5, s7
	s_cselect_b32 s33, s4, s6
	s_ashr_i32 s1, s0, 31
	s_lshl_b64 s[0:1], s[0:1], 24
	s_add_u32 s0, s33, s0
	s_addc_u32 s1, s31, s1
	s_or_b32 s2, s3, s2
	v_or_b32_e32 v0, s2, v142
	s_and_b32 s2, s30, 0x7c0
	v_or_b32_e32 v4, s2, v143
	v_lshlrev_b32_e32 v130, 2, v0
	v_lshl_add_u64 v[2:3], s[0:1], 0, v[130:131]
	v_lshlrev_b32_e32 v130, 13, v4
	v_lshl_add_u64 v[58:59], v[2:3], 0, v[130:131]
	v_add_co_u32_e32 v10, vcc, s11, v58
	s_nop 1
	v_addc_co_u32_e32 v11, vcc, 0, v59, vcc
	global_load_dwordx4 v[2:5], v[58:59], off nt
	global_load_dwordx4 v[6:9], v[10:11], off nt
	v_add_co_u32_e32 v10, vcc, s12, v58
	s_nop 1
	v_addc_co_u32_e32 v11, vcc, 0, v59, vcc
	v_add_co_u32_e32 v14, vcc, s13, v58
	s_nop 1
	v_addc_co_u32_e32 v15, vcc, 0, v59, vcc
	v_add_co_u32_e32 v18, vcc, s14, v58
	global_load_dwordx4 v[10:13], v[10:11], off nt
	s_nop 0
	global_load_dwordx4 v[14:17], v[14:15], off nt
	v_addc_co_u32_e32 v19, vcc, 0, v59, vcc
	v_add_co_u32_e32 v22, vcc, s16, v58
	s_nop 1
	v_addc_co_u32_e32 v23, vcc, 0, v59, vcc
	v_add_co_u32_e32 v26, vcc, s17, v58
	global_load_dwordx4 v[18:21], v[18:19], off nt
	s_nop 0
	global_load_dwordx4 v[22:25], v[22:23], off nt
	v_addc_co_u32_e32 v27, vcc, 0, v59, vcc
	v_add_co_u32_e32 v30, vcc, s18, v58
	s_nop 1
	v_addc_co_u32_e32 v31, vcc, 0, v59, vcc
	v_add_co_u32_e32 v34, vcc, s19, v58
	global_load_dwordx4 v[26:29], v[26:27], off nt
	s_nop 0
	global_load_dwordx4 v[30:33], v[30:31], off nt
	v_addc_co_u32_e32 v35, vcc, 0, v59, vcc
	v_add_co_u32_e32 v38, vcc, s20, v58
	s_nop 1
	v_addc_co_u32_e32 v39, vcc, 0, v59, vcc
	v_add_co_u32_e32 v42, vcc, s21, v58
	global_load_dwordx4 v[34:37], v[34:35], off nt
	s_nop 0
	global_load_dwordx4 v[38:41], v[38:39], off nt
	v_addc_co_u32_e32 v43, vcc, 0, v59, vcc
	v_add_co_u32_e32 v46, vcc, s22, v58
	s_nop 1
	v_addc_co_u32_e32 v47, vcc, 0, v59, vcc
	v_add_co_u32_e32 v50, vcc, 0x60000, v58
	global_load_dwordx4 v[42:45], v[42:43], off nt
	s_nop 0
	global_load_dwordx4 v[46:49], v[46:47], off nt
	v_addc_co_u32_e32 v51, vcc, 0, v59, vcc
	v_add_co_u32_e32 v54, vcc, 0x68000, v58
	s_nop 1
	v_addc_co_u32_e32 v55, vcc, 0, v59, vcc
	v_add_co_u32_e32 v60, vcc, 0x70000, v58
	global_load_dwordx4 v[50:53], v[50:51], off nt
	s_nop 0
	global_load_dwordx4 v[54:57], v[54:55], off nt
	v_addc_co_u32_e32 v61, vcc, 0, v59, vcc
	v_add_co_u32_e32 v62, vcc, 0x78000, v58
	s_nop 1
	v_addc_co_u32_e32 v63, vcc, 0, v59, vcc
	global_load_dwordx4 v[58:61], v[60:61], off nt
	s_nop 0
	global_load_dwordx4 v[62:65], v[62:63], off nt
	s_branch .Lc3_999

.LBB0_995:
	s_cmp_lg_u32 s89, 0
	s_cbranch_scc1 .LBB0_1002
	s_andn2_b64 vcc, exec, s[10:11]
	s_cbranch_vccnz .LBB0_1002
	s_sub_i32 s0, s82, s15
	s_lshl_b32 s25, s0, 3
	s_add_i32 s25, s25, s92
	s_cmpk_eq_i32 s88, 0x100
	s_cselect_b32 s98, 0x1800, 0
	s_add_i32 s25, s25, s98
	s_cmpk_gt_u32 s25, 0xa7ff
	s_cbranch_scc1 .LBB0_1002
	s_sub_i32 s0, s88, s15
	s_lshl_b32 s8, s0, 3
	s_add_u32 s9, s86, 0x50000000
	s_mul_i32 s0, s92, 0x4100
	s_addc_u32 s10, s87, 0
	s_load_dwordx2 s[4:5], s[90:91], 0xa0
	s_load_dwordx2 s[6:7], s[90:91], 0xb0
	s_add_i32 s2, s0, 0
	s_lshl_b32 s0, s25, 6
	s_lshl_b32 s1, s25, 5
	s_and_b32 s1, s1, 0x780
	s_and_b32 s0, s0, 64
	v_lshlrev_b32_e32 v0, 2, v1
	s_or_b32 s0, s1, s0
	s_waitcnt vmcnt(3)
	v_and_b32_e32 v142, 60, v0
	v_or_b32_e32 v0, s0, v142
	v_readlane_b32 s0, v255, 4
	s_bitcmp0_b32 s0, 7
	s_waitcnt lgkmcnt(0)
	s_cselect_b32 s1, s5, s7
	s_cselect_b32 s0, s4, s6
	s_lshl_b32 s3, s25, 13
	s_and_b32 s3, s3, 0x1f000000
	s_add_u32 s0, s0, s3
	s_addc_u32 s1, s1, 0
	s_and_b32 s3, s25, 0x7c0
	v_lshrrev_b32_e32 v143, 4, v1
	s_waitcnt vmcnt(0)
	v_or_b32_e32 v4, s3, v143
	v_lshlrev_b32_e32 v130, 2, v0
	v_mov_b32_e32 v131, 0
	v_lshl_add_u64 v[2:3], s[0:1], 0, v[130:131]
	v_lshlrev_b32_e32 v130, 13, v4
	v_lshl_add_u64 v[2:3], v[2:3], 0, v[130:131]
	s_mov_b32 s11, 0x8000
	v_add_co_u32_e32 v4, vcc, s11, v2
	s_mov_b32 s12, 0x10000
	s_nop 0
	v_addc_co_u32_e32 v5, vcc, 0, v3, vcc
	global_load_dwordx4 v[66:69], v[2:3], off nt
	global_load_dwordx4 v[70:73], v[4:5], off nt
	v_add_co_u32_e32 v4, vcc, s12, v2
	s_mov_b32 s13, 0x18000
	s_nop 0
	v_addc_co_u32_e32 v5, vcc, 0, v3, vcc
	v_add_co_u32_e32 v6, vcc, s13, v2
	s_mov_b32 s14, 0x20000
	s_nop 0
	v_addc_co_u32_e32 v7, vcc, 0, v3, vcc
	global_load_dwordx4 v[74:77], v[4:5], off nt
	global_load_dwordx4 v[78:81], v[6:7], off nt
	v_add_co_u32_e32 v4, vcc, s14, v2
	s_mov_b32 s16, 0x28000
	s_nop 0
	v_addc_co_u32_e32 v5, vcc, 0, v3, vcc
	v_add_co_u32_e32 v6, vcc, s16, v2
	s_mov_b32 s17, 0x30000
	s_nop 0
	v_addc_co_u32_e32 v7, vcc, 0, v3, vcc
	global_load_dwordx4 v[82:85], v[4:5], off nt
	global_load_dwordx4 v[86:89], v[6:7], off nt
	v_add_co_u32_e32 v4, vcc, s17, v2
	s_mov_b32 s18, 0x38000
	s_nop 0
	v_addc_co_u32_e32 v5, vcc, 0, v3, vcc
	v_add_co_u32_e32 v6, vcc, s18, v2
	s_mov_b32 s19, 0x40000
	s_nop 0
	v_addc_co_u32_e32 v7, vcc, 0, v3, vcc
	global_load_dwordx4 v[90:93], v[4:5], off nt
	global_load_dwordx4 v[94:97], v[6:7], off nt
	v_add_co_u32_e32 v4, vcc, s19, v2
	s_mov_b32 s20, 0x48000
	s_nop 0
	v_addc_co_u32_e32 v5, vcc, 0, v3, vcc
	v_add_co_u32_e32 v6, vcc, s20, v2
	s_mov_b32 s21, 0x50000
	s_nop 0
	v_addc_co_u32_e32 v7, vcc, 0, v3, vcc
	global_load_dwordx4 v[98:101], v[4:5], off nt
	global_load_dwordx4 v[102:105], v[6:7], off nt
	v_add_co_u32_e32 v4, vcc, s21, v2
	s_mov_b32 s22, 0x58000
	s_nop 0
	v_addc_co_u32_e32 v5, vcc, 0, v3, vcc
	v_add_co_u32_e32 v6, vcc, s22, v2
	s_mov_b32 s0, 0x60000
	s_nop 0
	v_addc_co_u32_e32 v7, vcc, 0, v3, vcc
	global_load_dwordx4 v[106:109], v[4:5], off nt
	global_load_dwordx4 v[110:113], v[6:7], off nt
	v_add_co_u32_e32 v4, vcc, s0, v2
	s_mov_b32 s0, 0x68000
	s_nop 0
	v_addc_co_u32_e32 v5, vcc, 0, v3, vcc
	v_add_co_u32_e32 v6, vcc, s0, v2
	s_mov_b32 s0, 0x70000
	s_nop 0
	v_addc_co_u32_e32 v7, vcc, 0, v3, vcc
	global_load_dwordx4 v[114:117], v[4:5], off nt
	global_load_dwordx4 v[118:121], v[6:7], off nt
	v_add_co_u32_e32 v4, vcc, s0, v2
	s_mov_b32 s0, 0x78000
	s_nop 0
	v_addc_co_u32_e32 v5, vcc, 0, v3, vcc
	v_add_co_u32_e32 v2, vcc, s0, v2
	s_lshl_b32 s0, s15, 3
	s_nop 0
	v_addc_co_u32_e32 v3, vcc, 0, v3, vcc
	global_load_dwordx4 v[122:125], v[4:5], off nt
	global_load_dwordx4 v[126:129], v[2:3], off nt
	s_sub_i32 s23, 0, s0
	s_lshl_b32 s0, s82, 3
	v_lshlrev_b32_e32 v3, 4, v1
	s_add_i32 s24, s92, s0
	s_add_i32 s24, s24, s98
	s_lshl_b32 s0, s88, 7
	s_lshl_b32 s1, s15, 7
	v_and_b32_e32 v132, 48, v3
	s_sub_i32 s26, s0, s1
	s_lshl_b32 s0, s88, 3
	s_lshl_b32 s1, s15, 4
	v_mul_u32_u24_e32 v3, 0x104, v132
	v_and_b32_e32 v4, 60, v1
	s_sub_i32 s27, s0, s1
	s_add_i32 s0, s24, s0
	v_add3_u32 v144, s2, v3, v4
	v_lshlrev_b32_e32 v3, 5, v1
	s_sub_i32 s0, s0, s1
	v_lshl_add_u32 v0, v142, 2, s2
	v_mul_u32_u24_e32 v2, 0x104, v143
	v_and_b32_e32 v134, 0x780, v3
	s_lshl_b32 s28, s0, 6
	s_lshl_b32 s0, s88, 9
	s_lshl_b32 s1, s15, 9
	v_mov_b32_e32 v133, v131
	v_mov_b32_e32 v135, v131
	v_or_b32_e32 v136, 0x800, v134
	v_mov_b32_e32 v137, v131
	v_or_b32_e32 v138, 0x1000, v134
	v_mov_b32_e32 v139, v131
	v_or_b32_e32 v140, 0x1800, v134
	v_mov_b32_e32 v141, v131
	s_lshl_b32 s25, s25, 4
	s_sub_i32 s15, s0, s1
	v_add_u32_e32 v145, v0, v2
	s_branch .LBB0_1000
.LBB0_999:
	v_add_u32_e32 v0, 0x410, v145
	s_waitcnt vmcnt(31)
	ds_write2_b32 v145, v66, v67 offset1:1
	ds_write2_b32 v145, v68, v69 offset0:2 offset1:3
	s_waitcnt vmcnt(30)
	ds_write2_b32 v0, v70, v71 offset1:1
	v_add_u32_e32 v0, 0x418, v145
	ds_write2_b32 v0, v72, v73 offset1:1
	v_add_u32_e32 v0, 0x820, v145
	s_waitcnt vmcnt(29)
	ds_write2_b32 v0, v74, v75 offset1:1
	v_add_u32_e32 v0, 0x828, v145
	ds_write2_b32 v0, v76, v77 offset1:1
	v_add_u32_e32 v0, 0xc30, v145
	s_waitcnt vmcnt(28)
	ds_write2_b32 v0, v78, v79 offset1:1
	v_add_u32_e32 v0, 0xc38, v145
	ds_write2_b32 v0, v80, v81 offset1:1
	v_add_u32_e32 v0, 0x1040, v145
	s_waitcnt vmcnt(27)
	ds_write2_b32 v0, v82, v83 offset1:1
	v_add_u32_e32 v0, 0x1048, v145
	ds_write2_b32 v0, v84, v85 offset1:1
	v_add_u32_e32 v0, 0x1450, v145
	s_waitcnt vmcnt(26)
	ds_write2_b32 v0, v86, v87 offset1:1
	v_add_u32_e32 v0, 0x1458, v145
	ds_write2_b32 v0, v88, v89 offset1:1
	v_add_u32_e32 v0, 0x1860, v145
	s_waitcnt vmcnt(25)
	ds_write2_b32 v0, v90, v91 offset1:1
	v_add_u32_e32 v0, 0x1868, v145
	ds_write2_b32 v0, v92, v93 offset1:1
	v_add_u32_e32 v0, 0x1c70, v145
	s_waitcnt vmcnt(24)
	ds_write2_b32 v0, v94, v95 offset1:1
	v_add_u32_e32 v0, 0x1c78, v145
	ds_write2_b32 v0, v96, v97 offset1:1
	v_add_u32_e32 v0, 0x2080, v145
	s_waitcnt vmcnt(23)
	ds_write2_b32 v0, v98, v99 offset1:1
	v_add_u32_e32 v0, 0x2088, v145
	ds_write2_b32 v0, v100, v101 offset1:1
	v_add_u32_e32 v0, 0x2490, v145
	s_waitcnt vmcnt(22)
	ds_write2_b32 v0, v102, v103 offset1:1
	v_add_u32_e32 v0, 0x2498, v145
	ds_write2_b32 v0, v104, v105 offset1:1
	v_add_u32_e32 v0, 0x28a0, v145
	s_waitcnt vmcnt(21)
	ds_write2_b32 v0, v106, v107 offset1:1
	v_add_u32_e32 v0, 0x28a8, v145
	ds_write2_b32 v0, v108, v109 offset1:1
	v_add_u32_e32 v0, 0x2cb0, v145
	s_waitcnt vmcnt(20)
	ds_write2_b32 v0, v110, v111 offset1:1
	v_add_u32_e32 v0, 0x2cb8, v145
	ds_write2_b32 v0, v112, v113 offset1:1
	v_add_u32_e32 v0, 0x30c0, v145
	s_waitcnt vmcnt(19)
	ds_write2_b32 v0, v114, v115 offset1:1
	v_add_u32_e32 v0, 0x30c8, v145
	ds_write2_b32 v0, v116, v117 offset1:1
	v_add_u32_e32 v0, 0x34d0, v145
	s_waitcnt vmcnt(18)
	ds_write2_b32 v0, v118, v119 offset1:1
	v_add_u32_e32 v0, 0x34d8, v145
	ds_write2_b32 v0, v120, v121 offset1:1
	v_add_u32_e32 v0, 0x38e0, v145
	s_waitcnt vmcnt(17)
	ds_write2_b32 v0, v122, v123 offset1:1
	v_add_u32_e32 v0, 0x38e8, v145
	ds_write2_b32 v0, v124, v125 offset1:1
	v_add_u32_e32 v0, 0x3cf0, v145
	s_waitcnt vmcnt(16)
	ds_write2_b32 v0, v126, v127 offset1:1
	v_add_u32_e32 v0, 0x3cf8, v145
	ds_write2_b32 v0, v128, v129 offset1:1
	s_waitcnt lgkmcnt(0)
	ds_read2_b32 v[70:71], v144 offset1:16
	ds_read2_b32 v[72:73], v144 offset0:65 offset1:81
	ds_read2_b32 v[74:75], v144 offset0:130 offset1:146
	ds_read2_b32 v[76:77], v144 offset0:195 offset1:211
	v_mov_b32_e32 v66, 0
	s_waitcnt lgkmcnt(3)
	v_mul_f32_e32 v0, 0x43800000, v70
	s_waitcnt lgkmcnt(2)
	v_mul_f32_e32 v67, 0x43800000, v72
	v_cvt_pk_fp8_f32 v66, v0, v67
	v_add_u32_e32 v0, 0x400, v144
	ds_read2_b32 v[78:79], v0 offset0:4 offset1:20
	ds_read2_b32 v[80:81], v0 offset0:69 offset1:85
	ds_read2_b32 v[82:83], v0 offset0:134 offset1:150
	s_waitcnt lgkmcnt(4)
	v_mul_f32_e32 v68, 0x43800000, v74
	s_waitcnt lgkmcnt(3)
	v_mul_f32_e32 v67, 0x43800000, v76
	ds_read2_b32 v[84:85], v0 offset0:199 offset1:215
	v_add_u32_e32 v106, 0x800, v144
	v_cvt_pk_fp8_f32 v66, v68, v67 op_sel:[0,0,1]
	s_waitcnt lgkmcnt(3)
	v_mul_f32_e32 v68, 0x43800000, v78
	s_waitcnt lgkmcnt(2)
	v_mul_f32_e32 v69, 0x43800000, v80
	v_mov_b32_e32 v67, 0
	ds_read2_b32 v[86:87], v106 offset0:8 offset1:24
	ds_read2_b32 v[88:89], v106 offset0:73 offset1:89
	v_add_u32_e32 v107, 0xc00, v144
	v_cvt_pk_fp8_f32 v67, v68, v69
	ds_read2_b32 v[90:91], v106 offset0:138 offset1:154
	ds_read2_b32 v[92:93], v106 offset0:203 offset1:219
	ds_read2_b32 v[94:95], v107 offset0:12 offset1:28
	ds_read2_b32 v[96:97], v107 offset0:77 offset1:93
	s_ashr_i32 s0, s29, 11
	s_ashr_i32 s1, s0, 31
	s_lshl_b64 s[0:1], s[0:1], 23
	s_waitcnt lgkmcnt(7)
	v_mul_f32_e32 v70, 0x43800000, v82
	s_waitcnt lgkmcnt(6)
	v_mul_f32_e32 v68, 0x43800000, v84
	s_add_u32 s0, s9, s0
	v_cvt_pk_fp8_f32 v67, v70, v68 op_sel:[0,0,1]
	s_waitcnt lgkmcnt(5)
	v_mul_f32_e32 v69, 0x43800000, v86
	s_waitcnt lgkmcnt(4)
	v_mul_f32_e32 v70, 0x43800000, v88
	v_mov_b32_e32 v68, 0
	ds_read2_b32 v[98:99], v107 offset0:142 offset1:158
	ds_read2_b32 v[100:101], v107 offset0:207 offset1:223
	s_addc_u32 s1, s10, s1
	s_and_b32 s2, s25, 0x3f0
	s_bfe_u32 s3, s29, 0x40007
	v_cvt_pk_fp8_f32 v68, v69, v70
	s_waitcnt lgkmcnt(3)
	v_mul_f32_e32 v70, 0x43800000, v94
	s_waitcnt lgkmcnt(2)
	v_mul_f32_e32 v76, 0x43800000, v96
	v_mov_b32_e32 v69, 0
	s_or_b32 s2, s2, s3
	v_cvt_pk_fp8_f32 v69, v70, v76
	s_lshl_b32 s2, s2, 13
	s_add_u32 s0, s0, s2
	v_mul_f32_e32 v72, 0x43800000, v90
	v_mul_f32_e32 v74, 0x43800000, v92
	s_addc_u32 s1, s1, 0
	s_and_b32 s2, s29, 64
	v_cvt_pk_fp8_f32 v68, v72, v74 op_sel:[0,0,1]
	s_waitcnt lgkmcnt(1)
	v_mul_f32_e32 v70, 0x43800000, v98
	s_waitcnt lgkmcnt(0)
	v_mul_f32_e32 v72, 0x43800000, v100
	s_add_u32 s0, s0, s2
	v_cvt_pk_fp8_f32 v69, v70, v72 op_sel:[0,0,1]
	s_addc_u32 s1, s1, 0
	v_lshl_add_u64 v[102:103], s[0:1], 0, v[132:133]
	v_lshl_add_u64 v[104:105], v[102:103], 0, v[134:135]
	global_store_dwordx4 v[104:105], v[66:69], off nt
	v_mul_f32_e32 v70, 0x43800000, v77
	v_mul_f32_e32 v72, 0x43800000, v93
	v_mul_f32_e32 v67, 0x43800000, v71
	v_mul_f32_e32 v68, 0x43800000, v73
	v_mov_b32_e32 v66, 0
	v_cvt_pk_fp8_f32 v66, v67, v68
	v_mul_f32_e32 v68, 0x43800000, v79
	v_mul_f32_e32 v71, 0x43800000, v81
	v_mov_b32_e32 v67, 0
	v_cvt_pk_fp8_f32 v67, v68, v71
	v_mul_f32_e32 v69, 0x43800000, v75
	v_cvt_pk_fp8_f32 v66, v69, v70 op_sel:[0,0,1]
	v_mul_f32_e32 v68, 0x43800000, v83
	v_mul_f32_e32 v69, 0x43800000, v85
	v_cvt_pk_fp8_f32 v67, v68, v69 op_sel:[0,0,1]
	v_mul_f32_e32 v69, 0x43800000, v87
	v_mul_f32_e32 v70, 0x43800000, v89
	v_mov_b32_e32 v68, 0
	v_cvt_pk_fp8_f32 v68, v69, v70
	v_mul_f32_e32 v70, 0x43800000, v95
	v_mul_f32_e32 v73, 0x43800000, v97
	v_mov_b32_e32 v69, 0
	v_cvt_pk_fp8_f32 v69, v70, v73
	v_mul_f32_e32 v71, 0x43800000, v91
	v_cvt_pk_fp8_f32 v68, v71, v72 op_sel:[0,0,1]
	v_mul_f32_e32 v70, 0x43800000, v99
	v_mul_f32_e32 v71, 0x43800000, v101
	v_cvt_pk_fp8_f32 v69, v70, v71 op_sel:[0,0,1]
	ds_read2_b32 v[70:71], v144 offset0:32 offset1:48
	ds_read2_b32 v[72:73], v144 offset0:97 offset1:113
	ds_read2_b32 v[74:75], v144 offset0:162 offset1:178
	v_lshl_add_u64 v[76:77], v[102:103], 0, v[136:137]
	s_add_i32 s24, s24, s8
	global_store_dwordx4 v[76:77], v[66:69], off nt
	ds_read2_b32 v[76:77], v144 offset0:227 offset1:243
	ds_read2_b32 v[78:79], v0 offset0:36 offset1:52
	ds_read2_b32 v[80:81], v0 offset0:101 offset1:117
	s_waitcnt lgkmcnt(5)
	v_mul_f32_e32 v67, 0x43800000, v70
	s_waitcnt lgkmcnt(4)
	v_mul_f32_e32 v68, 0x43800000, v72
	v_mov_b32_e32 v66, 0
	v_cvt_pk_fp8_f32 v66, v67, v68
	s_waitcnt lgkmcnt(3)
	v_mul_f32_e32 v69, 0x43800000, v74
	s_waitcnt lgkmcnt(2)
	v_mul_f32_e32 v67, 0x43800000, v76
	ds_read2_b32 v[82:83], v0 offset0:166 offset1:182
	ds_read2_b32 v[84:85], v0 offset0:231 offset1:247
	v_cvt_pk_fp8_f32 v66, v69, v67 op_sel:[0,0,1]
	s_waitcnt lgkmcnt(3)
	v_mul_f32_e32 v68, 0x43800000, v78
	s_waitcnt lgkmcnt(2)
	v_mul_f32_e32 v69, 0x43800000, v80
	v_mov_b32_e32 v67, 0
	ds_read2_b32 v[86:87], v106 offset0:40 offset1:56
	v_cvt_pk_fp8_f32 v67, v68, v69
	ds_read2_b32 v[88:89], v106 offset0:105 offset1:121
	ds_read2_b32 v[90:91], v106 offset0:170 offset1:186
	ds_read2_b32 v[92:93], v106 offset0:235 offset1:251
	ds_read2_b32 v[94:95], v107 offset0:44 offset1:60
	ds_read2_b32 v[96:97], v107 offset0:109 offset1:125
	s_waitcnt lgkmcnt(7)
	v_mul_f32_e32 v0, 0x43800000, v82
	s_waitcnt lgkmcnt(6)
	v_mul_f32_e32 v68, 0x43800000, v84
	v_cvt_pk_fp8_f32 v67, v0, v68 op_sel:[0,0,1]
	s_waitcnt lgkmcnt(5)
	v_mul_f32_e32 v0, 0x43800000, v86
	s_waitcnt lgkmcnt(4)
	v_mul_f32_e32 v69, 0x43800000, v88
	v_mov_b32_e32 v68, 0
	ds_read2_b32 v[98:99], v107 offset0:174 offset1:190
	ds_read2_b32 v[100:101], v107 offset0:239 offset1:255
	v_cvt_pk_fp8_f32 v68, v0, v69
	s_waitcnt lgkmcnt(3)
	v_mul_f32_e32 v0, 0x43800000, v94
	s_waitcnt lgkmcnt(2)
	v_mul_f32_e32 v74, 0x43800000, v96
	v_mov_b32_e32 v69, 0
	v_cvt_pk_fp8_f32 v69, v0, v74
	v_mul_f32_e32 v70, 0x43800000, v90
	v_mul_f32_e32 v72, 0x43800000, v92
	v_cvt_pk_fp8_f32 v68, v70, v72 op_sel:[0,0,1]
	s_waitcnt lgkmcnt(1)
	v_mul_f32_e32 v0, 0x43800000, v98
	s_waitcnt lgkmcnt(0)
	v_mul_f32_e32 v70, 0x43800000, v100
	v_cvt_pk_fp8_f32 v69, v0, v70 op_sel:[0,0,1]
	v_mul_f32_e32 v0, 0x43800000, v71
	v_mul_f32_e32 v71, 0x43800000, v73
	v_mov_b32_e32 v70, 0
	v_cvt_pk_fp8_f32 v70, v0, v71
	v_mul_f32_e32 v0, 0x43800000, v79
	v_mul_f32_e32 v74, 0x43800000, v81
	v_mov_b32_e32 v71, 0
	v_cvt_pk_fp8_f32 v71, v0, v74
	v_mul_f32_e32 v72, 0x43800000, v75
	v_mul_f32_e32 v73, 0x43800000, v77
	v_cvt_pk_fp8_f32 v70, v72, v73 op_sel:[0,0,1]
	v_mul_f32_e32 v0, 0x43800000, v83
	v_mul_f32_e32 v72, 0x43800000, v85
	v_cvt_pk_fp8_f32 v71, v0, v72 op_sel:[0,0,1]
	v_mul_f32_e32 v0, 0x43800000, v87
	v_mul_f32_e32 v73, 0x43800000, v89
	v_mov_b32_e32 v72, 0
	v_cvt_pk_fp8_f32 v72, v0, v73
	v_mul_f32_e32 v0, 0x43800000, v95
	v_mul_f32_e32 v76, 0x43800000, v97
	v_mov_b32_e32 v73, 0
	v_cvt_pk_fp8_f32 v73, v0, v76
	v_mul_f32_e32 v74, 0x43800000, v91
	v_mul_f32_e32 v75, 0x43800000, v93
	v_cvt_pk_fp8_f32 v72, v74, v75 op_sel:[0,0,1]
	v_mul_f32_e32 v0, 0x43800000, v99
	v_mul_f32_e32 v74, 0x43800000, v101
	v_cvt_pk_fp8_f32 v73, v0, v74 op_sel:[0,0,1]
	v_lshl_add_u64 v[74:75], v[102:103], 0, v[138:139]
	global_store_dwordx4 v[74:75], v[66:69], off nt
	s_add_i32 s0, s23, s24
	s_add_i32 s25, s25, s26
	v_lshl_add_u64 v[66:67], v[102:103], 0, v[140:141]
	global_store_dwordx4 v[66:67], v[70:73], off nt
	s_waitcnt lgkmcnt(0)
	s_add_i32 s28, s28, s15
	s_waitcnt vmcnt(4)
	v_mov_b64_e32 v[68:69], v[4:5]
	v_mov_b64_e32 v[72:73], v[8:9]
	v_mov_b64_e32 v[76:77], v[12:13]
	v_mov_b64_e32 v[80:81], v[16:17]
	v_mov_b64_e32 v[84:85], v[20:21]
	v_mov_b64_e32 v[88:89], v[24:25]
	v_mov_b64_e32 v[92:93], v[28:29]
	v_mov_b64_e32 v[96:97], v[32:33]
	v_mov_b64_e32 v[100:101], v[36:37]
	v_mov_b64_e32 v[104:105], v[40:41]
	v_mov_b64_e32 v[108:109], v[44:45]
	v_mov_b64_e32 v[112:113], v[48:49]
	v_mov_b64_e32 v[116:117], v[52:53]
	v_mov_b64_e32 v[120:121], v[56:57]
	v_mov_b64_e32 v[124:125], v[60:61]
	v_mov_b64_e32 v[128:129], v[64:65]
	s_cmp_lt_i32 s0, 0xa800
	v_mov_b64_e32 v[66:67], v[2:3]
	v_mov_b64_e32 v[70:71], v[6:7]
	v_mov_b64_e32 v[74:75], v[10:11]
	v_mov_b64_e32 v[78:79], v[14:15]
	v_mov_b64_e32 v[82:83], v[18:19]
	v_mov_b64_e32 v[86:87], v[22:23]
	v_mov_b64_e32 v[90:91], v[26:27]
	v_mov_b64_e32 v[94:95], v[30:31]
	v_mov_b64_e32 v[98:99], v[34:35]
	v_mov_b64_e32 v[102:103], v[38:39]
	v_mov_b64_e32 v[106:107], v[42:43]
	v_mov_b64_e32 v[110:111], v[46:47]
	v_mov_b64_e32 v[114:115], v[50:51]
	v_mov_b64_e32 v[118:119], v[54:55]
	v_mov_b64_e32 v[122:123], v[58:59]
	v_mov_b64_e32 v[126:127], v[62:63]
	s_cbranch_scc0 .LBB0_1002
.LBB0_1000:
	s_add_i32 s29, s23, s24
	s_add_i32 s30, s27, s24
	s_cmp_gt_i32 s30, 0xa7ff
	s_cbranch_scc1 .Lcv4_last
	s_lshr_b32 s1, s28, 1
	s_ashr_i32 s0, s30, 11
	s_and_b32 s2, s1, 0x780
	s_and_b32 s3, s28, 64
	s_bitcmp0_b32 s29, 1
	s_cselect_b32 s31, s5, s7
	s_cselect_b32 s33, s4, s6
	s_ashr_i32 s1, s0, 31
	s_lshl_b64 s[0:1], s[0:1], 24
	s_add_u32 s0, s33, s0
	s_addc_u32 s1, s31, s1
	s_or_b32 s2, s3, s2
	v_or_b32_e32 v0, s2, v142
	s_and_b32 s2, s30, 0x7c0
	v_or_b32_e32 v4, s2, v143
	v_lshlrev_b32_e32 v130, 2, v0
	v_lshl_add_u64 v[2:3], s[0:1], 0, v[130:131]
	v_lshlrev_b32_e32 v130, 13, v4
	v_lshl_add_u64 v[58:59], v[2:3], 0, v[130:131]
	v_add_co_u32_e32 v10, vcc, s11, v58
	s_nop 1
	v_addc_co_u32_e32 v11, vcc, 0, v59, vcc
	global_load_dwordx4 v[2:5], v[58:59], off nt
	global_load_dwordx4 v[6:9], v[10:11], off nt
	v_add_co_u32_e32 v10, vcc, s12, v58
	s_nop 1
	v_addc_co_u32_e32 v11, vcc, 0, v59, vcc
	v_add_co_u32_e32 v14, vcc, s13, v58
	s_nop 1
	v_addc_co_u32_e32 v15, vcc, 0, v59, vcc
	v_add_co_u32_e32 v18, vcc, s14, v58
	global_load_dwordx4 v[10:13], v[10:11], off nt
	s_nop 0
	global_load_dwordx4 v[14:17], v[14:15], off nt
	v_addc_co_u32_e32 v19, vcc, 0, v59, vcc
	v_add_co_u32_e32 v22, vcc, s16, v58
	s_nop 1
	v_addc_co_u32_e32 v23, vcc, 0, v59, vcc
	v_add_co_u32_e32 v26, vcc, s17, v58
	global_load_dwordx4 v[18:21], v[18:19], off nt
	s_nop 0
	global_load_dwordx4 v[22:25], v[22:23], off nt
	v_addc_co_u32_e32 v27, vcc, 0, v59, vcc
	v_add_co_u32_e32 v30, vcc, s18, v58
	s_nop 1
	v_addc_co_u32_e32 v31, vcc, 0, v59, vcc
	v_add_co_u32_e32 v34, vcc, s19, v58
	global_load_dwordx4 v[26:29], v[26:27], off nt
	s_nop 0
	global_load_dwordx4 v[30:33], v[30:31], off nt
	v_addc_co_u32_e32 v35, vcc, 0, v59, vcc
	v_add_co_u32_e32 v38, vcc, s20, v58
	s_nop 1
	v_addc_co_u32_e32 v39, vcc, 0, v59, vcc
	v_add_co_u32_e32 v42, vcc, s21, v58
	global_load_dwordx4 v[34:37], v[34:35], off nt
	s_nop 0
	global_load_dwordx4 v[38:41], v[38:39], off nt
	v_addc_co_u32_e32 v43, vcc, 0, v59, vcc
	v_add_co_u32_e32 v46, vcc, s22, v58
	s_nop 1
	v_addc_co_u32_e32 v47, vcc, 0, v59, vcc
	v_add_co_u32_e32 v50, vcc, 0x60000, v58
	global_load_dwordx4 v[42:45], v[42:43], off nt
	s_nop 0
	global_load_dwordx4 v[46:49], v[46:47], off nt
	v_addc_co_u32_e32 v51, vcc, 0, v59, vcc
	v_add_co_u32_e32 v54, vcc, 0x68000, v58
	s_nop 1
	v_addc_co_u32_e32 v55, vcc, 0, v59, vcc
	v_add_co_u32_e32 v60, vcc, 0x70000, v58
	global_load_dwordx4 v[50:53], v[50:51], off nt
	s_nop 0
	global_load_dwordx4 v[54:57], v[54:55], off nt
	v_addc_co_u32_e32 v61, vcc, 0, v59, vcc
	v_add_co_u32_e32 v62, vcc, 0x78000, v58
	s_nop 1
	v_addc_co_u32_e32 v63, vcc, 0, v59, vcc
	global_load_dwordx4 v[58:61], v[60:61], off nt
	s_nop 0
	global_load_dwordx4 v[62:65], v[62:63], off nt
	s_branch .LBB0_999

.LBB0_1311:
	s_lshl_b32 s0, s82, 2
	s_add_i32 s0, s0, s92
	s_add_i32 s0, s0, -4
	s_cmpk_gt_u32 s1, 0xff
	s_cselect_b32 s14, s0, -1
	s_cmp_lt_i32 s14, 0
	s_cbranch_scc1 .LBB0_1329
	s_cmpk_gt_u32 s88, 0xe0
	s_mov_b32 s0, 0x10000
	s_cselect_b32 s0, s0, 0x16000
	s_cmpk_gt_i32 s88, 0xab
	s_cselect_b32 s1, 0xa800, 0
	s_cselect_b32 s18, s0, 0x18000
	s_add_i32 s19, s14, s1
	s_cmp_ge_u32 s19, s18
	s_cbranch_scc1 .LBB0_1329
	s_load_dwordx2 s[4:5], s[90:91], 0xa0
	s_load_dwordx2 s[6:7], s[90:91], 0xb0
	s_load_dwordx2 s[8:9], s[90:91], 0xc0
	s_cmpk_gt_u32 s19, 0xffff
	v_readfirstlane_b32 s34, v0
	s_waitcnt vmcnt(0)
	v_lshlrev_b32_e32 v2, 2, v1
	s_cbranch_scc0 .LBB0_1315
	s_add_i32 s34, s19, 0xffff0000
	s_lshr_b32 s0, s34, 10
	s_mov_b32 s1, 0
	s_lshl_b64 s[0:1], s[0:1], 24
	s_waitcnt lgkmcnt(0)
	s_add_u32 s10, s8, s0
	s_addc_u32 s11, s9, s1
	s_lshl_b32 s1, s19, 6
	s_lshl_b32 s0, s19, 1
	s_and_b32 s1, s1, 0x7c0
	v_and_b32_e32 v142, 60, v2
	v_or_b32_e32 v130, s1, v142
	v_mov_b32_e32 v143, s0
	v_mov_b32_e32 v3, v143
	s_cbranch_execz .LBB0_1316
	s_branch .LBB0_1317
